# plus non-temporal stores for the fp8 row copies of the prologue
# speedup vs baseline: 1.0131x; 1.0040x over previous
.LBB0_13:
	s_mov_b64 s[6:7], s[0:1]
	s_load_dwordx2 s[26:27], s[6:7], 0x0
	s_mov_b64 s[6:7], s[0:1]
	s_add_i32 s8, s31, 0x4000
	s_ashr_i32 s9, s8, 31
	s_waitcnt lgkmcnt(0)
	v_lshl_add_u64 v[2:3], s[26:27], 0, v[52:53]
	global_load_dwordx4 v[34:37], v[2:3], off offset:-4096 nt
	global_load_dwordx4 v[30:33], v[2:3], off offset:-3072 nt
	global_load_dwordx4 v[18:21], v[2:3], off offset:-2048 nt
	global_load_dwordx4 v[10:13], v[2:3], off offset:-1024 nt
	s_load_dwordx2 s[26:27], s[6:7], 0x0
	s_lshl_b64 s[6:7], s[8:9], 11
	s_lshl_b64 s[34:35], s[8:9], 13
	v_add_co_u32_e32 v4, vcc, s3, v2
	s_waitcnt lgkmcnt(0)
	s_add_u32 s26, s26, s34
	s_addc_u32 s27, s27, s35
	v_addc_co_u32_e32 v5, vcc, -1, v3, vcc
	v_lshl_add_u64 v[6:7], s[26:27], 0, v[42:43]
	global_load_dwordx4 v[66:69], v[4:5], off offset:-3072 nt
	global_load_dwordx4 v[70:73], v[4:5], off offset:-2048 nt
	v_add_co_u32_e32 v90, vcc, s13, v6
	global_load_dwordx4 v[74:77], v[4:5], off offset:-1024 nt
	s_nop 0
	v_addc_co_u32_e32 v91, vcc, 0, v7, vcc
	global_load_dwordx4 v[2:5], v[2:3], off nt
	s_nop 0
	global_load_dwordx4 v[78:81], v42, s[26:27] nt
	global_load_dwordx4 v[82:85], v42, s[26:27] offset:1024 nt
	global_load_dwordx4 v[86:89], v42, s[26:27] offset:2048 nt
	global_load_dwordx4 v[38:41], v42, s[26:27] offset:3072 nt
	global_load_dwordx4 v[26:29], v[90:91], off nt
	global_load_dwordx4 v[22:25], v[90:91], off offset:1024 nt
	global_load_dwordx4 v[14:17], v[90:91], off offset:2048 nt
	global_load_dwordx4 v[6:9], v[90:91], off offset:3072 nt
	v_lshl_add_u64 v[90:91], s[82:83], 0, v[48:49]
	v_add_co_u32_e32 v90, vcc, s15, v90
	s_lshl_b64 s[8:9], s[8:9], 12
	s_nop 0
	v_addc_co_u32_e32 v91, vcc, 0, v91, vcc
	v_lshl_add_u64 v[92:93], v[44:45], 0, s[8:9]
	s_waitcnt vmcnt(15)
	v_cvt_pk_bf16_f32 v94, v34, v35
	v_cvt_pk_bf16_f32 v95, v36, v37
	s_waitcnt vmcnt(14)
	v_cvt_pk_bf16_f32 v96, v30, v31
	v_cvt_pk_bf16_f32 v97, v32, v33
	s_waitcnt vmcnt(13)
	v_cvt_pk_bf16_f32 v98, v18, v19
	v_cvt_pk_bf16_f32 v99, v20, v21
	s_waitcnt vmcnt(12)
	v_cvt_pk_bf16_f32 v100, v10, v11
	v_cvt_pk_bf16_f32 v101, v12, v13
	s_waitcnt vmcnt(11)
	v_cvt_pk_bf16_f32 v102, v66, v67
	v_cvt_pk_bf16_f32 v103, v68, v69
	s_waitcnt vmcnt(10)
	v_cvt_pk_bf16_f32 v105, v72, v73
	global_store_dwordx2 v[90:91], v[102:103], off nt
	v_cvt_pk_bf16_f32 v104, v70, v71
	s_waitcnt vmcnt(8)
	v_cvt_pk_bf16_f32 v102, v78, v79
	v_cvt_pk_bf16_f32 v103, v80, v81
	v_cvt_pk_bf16_f32 v106, v74, v75
	v_cvt_pk_bf16_f32 v107, v76, v77
	v_mul_f32_e32 v116, v67, v67
	s_waitcnt vmcnt(7)
	v_cvt_pk_bf16_f32 v110, v82, v83
	v_cvt_pk_bf16_f32 v111, v84, v85
	s_waitcnt vmcnt(6)
	v_cvt_pk_bf16_f32 v112, v86, v87
	v_cvt_pk_bf16_f32 v113, v88, v89
	s_waitcnt vmcnt(5)
	v_cvt_pk_bf16_f32 v114, v38, v39
	v_cvt_pk_bf16_f32 v115, v40, v41
	global_store_dwordx2 v[92:93], v[102:103], off nt
	global_store_dwordx2 v[90:91], v[104:105], off offset:512 nt
	global_store_dwordx2 v[92:93], v[110:111], off offset:512 nt
	global_store_dwordx2 v[90:91], v[106:107], off offset:1024 nt
	global_store_dwordx2 v[92:93], v[112:113], off offset:1024 nt
	global_store_dwordx2 v[90:91], v[94:95], off offset:1536 nt
	global_store_dwordx2 v[92:93], v[114:115], off offset:1536 nt
	global_store_dwordx2 v[90:91], v[96:97], off offset:2048 nt
	s_waitcnt vmcnt(12)
	v_cvt_pk_bf16_f32 v94, v26, v27
	v_cvt_pk_bf16_f32 v95, v28, v29
	s_waitcnt vmcnt(9)
	v_cvt_pk_bf16_f32 v105, v8, v9
	v_cvt_pk_bf16_f32 v108, v2, v3
	v_cvt_pk_bf16_f32 v109, v4, v5
	v_cvt_pk_bf16_f32 v96, v22, v23
	v_cvt_pk_bf16_f32 v97, v24, v25
	v_cvt_pk_bf16_f32 v102, v14, v15
	v_cvt_pk_bf16_f32 v103, v16, v17
	v_cvt_pk_bf16_f32 v104, v6, v7
	global_store_dwordx2 v[92:93], v[94:95], off offset:2048 nt
	global_store_dwordx2 v[90:91], v[98:99], off offset:2560 nt
	global_store_dwordx2 v[92:93], v[96:97], off offset:2560 nt
	global_store_dwordx2 v[90:91], v[100:101], off offset:3072 nt
	global_store_dwordx2 v[92:93], v[102:103], off offset:3072 nt
	global_store_dwordx2 v[90:91], v[108:109], off offset:3584 nt
	global_store_dwordx2 v[92:93], v[104:105], off offset:3584 nt
	v_fmac_f32_e32 v116, v66, v66
	v_mul_f32_e32 v90, v69, v69
	v_mul_f32_e32 v66, 4.0, v66
	v_mul_f32_e32 v67, 4.0, v67
	v_mul_f32_e32 v91, v79, v79
	v_mul_f32_e32 v105, v31, v31
	v_fmac_f32_e32 v90, v68, v68
	v_mul_f32_e32 v68, 4.0, v68
	v_mul_f32_e32 v69, 4.0, v69
	v_fmac_f32_e32 v91, v78, v78
	v_mul_f32_e32 v78, 4.0, v78
	v_mul_f32_e32 v79, 4.0, v79
	v_mul_f32_e32 v93, v71, v71
	v_fmac_f32_e32 v105, v30, v30
	v_mul_f32_e32 v107, 4.0, v30
	v_mul_f32_e32 v108, 4.0, v31
	v_med3_f32 v30, v66, s28, v61
	v_med3_f32 v31, v67, s28, v61
	v_mov_b32_e32 v66, 0
	v_fmac_f32_e32 v93, v70, v70
	v_mul_f32_e32 v70, 4.0, v70
	v_mul_f32_e32 v71, 4.0, v71
	v_cvt_pk_fp8_f32 v66, v30, v31
	v_med3_f32 v30, v68, s28, v61
	v_med3_f32 v31, v69, s28, v61
	v_med3_f32 v67, v78, s28, v61
	v_med3_f32 v68, v79, s28, v61
	v_mov_b32_e32 v69, 0
	v_cvt_pk_fp8_f32 v69, v67, v68
	v_med3_f32 v67, v70, s28, v61
	v_med3_f32 v68, v71, s28, v61
	v_mov_b32_e32 v70, 0
	v_mul_f32_e32 v92, v81, v81
	v_cvt_pk_fp8_f32 v70, v67, v68
	v_fmac_f32_e32 v92, v80, v80
	v_mul_f32_e32 v80, 4.0, v80
	v_mul_f32_e32 v81, 4.0, v81
	v_mul_f32_e32 v94, v73, v73
	v_fmac_f32_e32 v94, v72, v72
	v_mul_f32_e32 v72, 4.0, v72
	v_mul_f32_e32 v73, 4.0, v73
	v_mul_f32_e32 v95, v83, v83
	v_med3_f32 v67, v80, s28, v61
	v_med3_f32 v68, v81, s28, v61
	v_fmac_f32_e32 v95, v82, v82
	v_mul_f32_e32 v82, 4.0, v82
	v_mul_f32_e32 v83, 4.0, v83
	v_mul_f32_e32 v97, v75, v75
	v_cvt_pk_fp8_f32 v69, v67, v68 op_sel:[0,0,1]
	v_med3_f32 v67, v72, s28, v61
	v_med3_f32 v68, v73, s28, v61
	v_fmac_f32_e32 v97, v74, v74
	v_mul_f32_e32 v74, 4.0, v74
	v_mul_f32_e32 v75, 4.0, v75
	v_cvt_pk_fp8_f32 v70, v67, v68 op_sel:[0,0,1]
	v_med3_f32 v67, v82, s28, v61
	v_med3_f32 v68, v83, s28, v61
	v_mov_b32_e32 v71, 0
	v_cvt_pk_fp8_f32 v71, v67, v68
	v_med3_f32 v67, v74, s28, v61
	v_med3_f32 v68, v75, s28, v61
	v_mov_b32_e32 v72, 0
	v_mul_f32_e32 v96, v85, v85
	v_cvt_pk_fp8_f32 v72, v67, v68
	v_fmac_f32_e32 v96, v84, v84
	v_mul_f32_e32 v84, 4.0, v84
	v_mul_f32_e32 v85, 4.0, v85
	v_mul_f32_e32 v98, v77, v77
	v_fmac_f32_e32 v98, v76, v76
	v_mul_f32_e32 v76, 4.0, v76
	v_mul_f32_e32 v77, 4.0, v77
	v_mul_f32_e32 v99, v87, v87
	v_med3_f32 v67, v84, s28, v61
	v_med3_f32 v68, v85, s28, v61
	v_fmac_f32_e32 v99, v86, v86
	v_mul_f32_e32 v86, 4.0, v86
	v_mul_f32_e32 v87, 4.0, v87
	v_mul_f32_e32 v101, v35, v35
	v_cvt_pk_fp8_f32 v71, v67, v68 op_sel:[0,0,1]
	v_med3_f32 v67, v76, s28, v61
	v_med3_f32 v68, v77, s28, v61
	v_fmac_f32_e32 v101, v34, v34
	v_mul_f32_e32 v34, 4.0, v34
	v_mul_f32_e32 v35, 4.0, v35
	v_cvt_pk_fp8_f32 v72, v67, v68 op_sel:[0,0,1]
	v_med3_f32 v67, v86, s28, v61
	v_med3_f32 v68, v87, s28, v61
	v_mov_b32_e32 v73, 0
	v_cvt_pk_fp8_f32 v73, v67, v68
	v_med3_f32 v34, v34, s28, v61
	v_med3_f32 v35, v35, s28, v61
	v_mov_b32_e32 v67, 0
	v_mul_f32_e32 v100, v89, v89
	v_cvt_pk_fp8_f32 v67, v34, v35
	v_fmac_f32_e32 v100, v88, v88
	v_mul_f32_e32 v88, 4.0, v88
	v_mul_f32_e32 v89, 4.0, v89
	v_mul_f32_e32 v102, v37, v37
	v_fmac_f32_e32 v102, v36, v36
	v_mul_f32_e32 v36, 4.0, v36
	v_mul_f32_e32 v37, 4.0, v37
	v_mul_f32_e32 v103, v39, v39
	v_med3_f32 v34, v88, s28, v61
	v_med3_f32 v35, v89, s28, v61
	v_fmac_f32_e32 v103, v38, v38
	v_mul_f32_e32 v38, 4.0, v38
	v_mul_f32_e32 v39, 4.0, v39
	v_cvt_pk_fp8_f32 v73, v34, v35 op_sel:[0,0,1]
	v_med3_f32 v34, v36, s28, v61
	v_med3_f32 v35, v37, s28, v61
	v_cvt_pk_fp8_f32 v67, v34, v35 op_sel:[0,0,1]
	v_med3_f32 v34, v38, s28, v61
	v_med3_f32 v35, v39, s28, v61
	v_mov_b32_e32 v36, 0
	v_cvt_pk_fp8_f32 v36, v34, v35
	v_mul_f32_e32 v104, v41, v41
	v_fmac_f32_e32 v104, v40, v40
	v_mul_f32_e32 v40, 4.0, v40
	v_mul_f32_e32 v41, 4.0, v41
	v_med3_f32 v34, v107, s28, v61
	v_med3_f32 v35, v108, s28, v61
	v_mov_b32_e32 v37, 0
	v_cvt_pk_fp8_f32 v37, v34, v35
	v_med3_f32 v34, v40, s28, v61
	v_med3_f32 v35, v41, s28, v61
	v_cvt_pk_fp8_f32 v36, v34, v35 op_sel:[0,0,1]
	v_add_f32_e32 v34, v116, v90
	v_add_f32_e32 v38, v93, v94
	v_add_f32_e32 v35, v91, v92
	v_add_f32_e32 v34, v34, v38
	v_add_f32_e32 v38, v95, v96
	v_add_f32_e32 v35, v35, v38
	v_add_f32_e32 v38, v97, v98
	v_add_f32_e32 v34, v34, v38
	v_add_f32_e32 v38, v99, v100
	v_mul_f32_e32 v106, v33, v33
	v_add_f32_e32 v35, v35, v38
	v_add_f32_e32 v38, v101, v102
	v_fmac_f32_e32 v106, v32, v32
	v_add_f32_e32 v34, v34, v38
	v_add_f32_e32 v38, v103, v104
	v_add_f32_e32 v35, v35, v38
	v_add_f32_e32 v38, v105, v106
	v_add_f32_e32 v34, v34, v38
	v_mul_f32_e32 v38, v27, v27
	v_mul_f32_e32 v39, v29, v29
	v_fmac_f32_e32 v38, v26, v26
	v_fmac_f32_e32 v39, v28, v28
	v_add_f32_e32 v38, v38, v39
	v_add_f32_e32 v35, v35, v38
	v_mul_f32_e32 v38, v19, v19
	v_mul_f32_e32 v39, v21, v21
	v_fmac_f32_e32 v38, v18, v18
	v_fmac_f32_e32 v39, v20, v20
	v_add_f32_e32 v38, v38, v39
	v_add_f32_e32 v34, v34, v38
	v_mul_f32_e32 v38, v23, v23
	v_mul_f32_e32 v39, v25, v25
	v_fmac_f32_e32 v38, v22, v22
	v_fmac_f32_e32 v39, v24, v24
	v_add_f32_e32 v38, v38, v39
	v_cvt_pk_fp8_f32 v66, v30, v31 op_sel:[0,0,1]
	v_lshl_add_u64 v[30:31], s[82:83], 0, v[50:51]
	v_add_f32_e32 v35, v35, v38
	v_mul_f32_e32 v38, v11, v11
	v_mul_f32_e32 v39, v13, v13
	v_add_co_u32_e32 v30, vcc, s29, v30
	v_fmac_f32_e32 v38, v10, v10
	v_fmac_f32_e32 v39, v12, v12
	v_mul_f32_e32 v40, v3, v3
	v_mul_f32_e32 v41, v5, v5
	v_addc_co_u32_e32 v31, vcc, 0, v31, vcc
	v_add_f32_e32 v38, v38, v39
	v_fmac_f32_e32 v40, v2, v2
	v_fmac_f32_e32 v41, v4, v4
	v_add_f32_e32 v34, v34, v38
	v_add_f32_e32 v40, v40, v41
	v_cmp_lt_i32_e32 vcc, v55, v54
	v_add_f32_e32 v34, v34, v40
	v_mul_f32_e32 v38, v15, v15
	v_cndmask_b32_e32 v40, v1, v55, vcc
	v_lshlrev_b32_e32 v40, 2, v40
	ds_bpermute_b32 v41, v40, v34
	v_mul_f32_e32 v39, v17, v17
	v_fmac_f32_e32 v38, v14, v14
	v_fmac_f32_e32 v39, v16, v16
	v_cmp_lt_i32_e32 vcc, v56, v54
	v_add_f32_e32 v38, v38, v39
	s_waitcnt lgkmcnt(0)
	v_add_f32_e32 v34, v34, v41
	v_cndmask_b32_e32 v39, v1, v56, vcc
	v_lshlrev_b32_e32 v39, 2, v39
	ds_bpermute_b32 v41, v39, v34
	v_add_f32_e32 v35, v35, v38
	v_mul_f32_e32 v38, v7, v7
	v_mul_f32_e32 v68, v9, v9
	v_fmac_f32_e32 v38, v6, v6
	v_fmac_f32_e32 v68, v8, v8
	v_add_f32_e32 v38, v38, v68
	v_cmp_lt_i32_e32 vcc, v57, v54
	v_add_f32_e32 v35, v35, v38
	s_waitcnt lgkmcnt(0)
	v_add_f32_e32 v34, v34, v41
	v_cndmask_b32_e32 v38, v1, v57, vcc
	v_lshlrev_b32_e32 v38, 2, v38
	ds_bpermute_b32 v40, v40, v35
	ds_bpermute_b32 v41, v38, v34
	v_mul_f32_e32 v32, 4.0, v32
	v_mul_f32_e32 v33, 4.0, v33
	v_med3_f32 v32, v32, s28, v61
	v_med3_f32 v33, v33, s28, v61
	v_cmp_lt_i32_e32 vcc, v58, v54
	v_cvt_pk_fp8_f32 v37, v32, v33 op_sel:[0,0,1]
	s_waitcnt lgkmcnt(1)
	v_add_f32_e32 v33, v35, v40
	v_cndmask_b32_e32 v35, v1, v58, vcc
	s_waitcnt lgkmcnt(0)
	v_add_f32_e32 v32, v34, v41
	v_lshlrev_b32_e32 v35, 2, v35
	ds_bpermute_b32 v34, v39, v33
	ds_bpermute_b32 v39, v35, v32
	v_mul_f32_e32 v26, 4.0, v26
	v_mul_f32_e32 v27, 4.0, v27
	v_med3_f32 v26, v26, s28, v61
	v_med3_f32 v27, v27, s28, v61
	s_waitcnt lgkmcnt(0)
	v_add_f32_e32 v32, v32, v39
	v_mov_b32_e32 v39, 0
	v_cvt_pk_fp8_f32 v39, v26, v27
	v_mul_f32_e32 v28, 4.0, v28
	v_mul_f32_e32 v29, 4.0, v29
	v_med3_f32 v28, v28, s28, v61
	v_med3_f32 v29, v29, s28, v61
	v_mul_f32_e32 v18, 4.0, v18
	v_mul_f32_e32 v19, 4.0, v19
	v_cvt_pk_fp8_f32 v39, v28, v29 op_sel:[0,0,1]
	v_med3_f32 v18, v18, s28, v61
	v_med3_f32 v19, v19, s28, v61
	v_mov_b32_e32 v28, 0
	v_cvt_pk_fp8_f32 v28, v18, v19
	v_mul_f32_e32 v20, 4.0, v20
	v_mul_f32_e32 v18, 4.0, v21
	v_med3_f32 v19, v20, s28, v61
	v_med3_f32 v18, v18, s28, v61
	v_cvt_pk_fp8_f32 v28, v19, v18 op_sel:[0,0,1]
	v_mul_f32_e32 v18, 4.0, v22
	v_mul_f32_e32 v19, 4.0, v23
	v_med3_f32 v18, v18, s28, v61
	v_med3_f32 v19, v19, s28, v61
	v_mov_b32_e32 v21, 0
	v_cvt_pk_fp8_f32 v21, v18, v19
	v_mul_f32_e32 v20, 4.0, v24
	v_mul_f32_e32 v18, 4.0, v25
	v_add_f32_e32 v33, v33, v34
	v_med3_f32 v19, v20, s28, v61
	v_med3_f32 v18, v18, s28, v61
	v_mul_f32_e32 v10, 4.0, v10
	v_mul_f32_e32 v11, 4.0, v11
	ds_bpermute_b32 v34, v38, v33
	v_cvt_pk_fp8_f32 v21, v19, v18 op_sel:[0,0,1]
	v_med3_f32 v10, v10, s28, v61
	v_med3_f32 v11, v11, s28, v61
	v_mov_b32_e32 v18, 0
	v_cvt_pk_fp8_f32 v18, v10, v11
	v_mul_f32_e32 v12, 4.0, v12
	v_mul_f32_e32 v10, 4.0, v13
	v_med3_f32 v11, v12, s28, v61
	v_med3_f32 v10, v10, s28, v61
	s_waitcnt lgkmcnt(0)
	v_add_f32_e32 v33, v33, v34
	v_cvt_pk_fp8_f32 v18, v11, v10 op_sel:[0,0,1]
	v_mul_f32_e32 v10, 4.0, v14
	v_mul_f32_e32 v11, 4.0, v15
	ds_bpermute_b32 v34, v35, v33
	v_med3_f32 v10, v10, s28, v61
	v_med3_f32 v11, v11, s28, v61
	v_mov_b32_e32 v13, 0
	v_cvt_pk_fp8_f32 v13, v10, v11
	v_cmp_lt_i32_e32 vcc, v59, v54
	v_mul_f32_e32 v12, 4.0, v16
	v_mul_f32_e32 v10, 4.0, v17
	v_cndmask_b32_e32 v35, v1, v59, vcc
	v_med3_f32 v11, v12, s28, v61
	v_med3_f32 v10, v10, s28, v61
	v_mul_f32_e32 v2, 4.0, v2
	v_mul_f32_e32 v3, 4.0, v3
	v_lshlrev_b32_e32 v35, 2, v35
	s_waitcnt lgkmcnt(0)
	v_add_f32_e32 v33, v33, v34
	v_cvt_pk_fp8_f32 v13, v11, v10 op_sel:[0,0,1]
	v_med3_f32 v2, v2, s28, v61
	v_med3_f32 v3, v3, s28, v61
	v_mov_b32_e32 v10, 0
	ds_bpermute_b32 v38, v35, v32
	ds_bpermute_b32 v34, v35, v33
	v_cvt_pk_fp8_f32 v10, v2, v3
	v_mul_f32_e32 v4, 4.0, v4
	v_mul_f32_e32 v2, 4.0, v5
	v_cmp_lt_i32_e32 vcc, v60, v54
	v_med3_f32 v3, v4, s28, v61
	v_med3_f32 v2, v2, s28, v61
	v_cndmask_b32_e32 v27, v1, v60, vcc
	v_cvt_pk_fp8_f32 v10, v3, v2 op_sel:[0,0,1]
	v_mul_f32_e32 v2, 4.0, v6
	v_mul_f32_e32 v3, 4.0, v7
	s_waitcnt lgkmcnt(1)
	v_add_f32_e32 v32, v32, v38
	s_waitcnt lgkmcnt(0)
	v_add_f32_e32 v26, v33, v34
	v_lshlrev_b32_e32 v27, 2, v27
	v_med3_f32 v2, v2, s28, v61
	v_med3_f32 v3, v3, s28, v61
	v_mov_b32_e32 v5, 0
	ds_bpermute_b32 v33, v27, v32
	ds_bpermute_b32 v27, v27, v26
	v_cvt_pk_fp8_f32 v5, v2, v3
	v_mul_f32_e32 v4, 4.0, v8
	v_mul_f32_e32 v2, 4.0, v9
	v_med3_f32 v3, v4, s28, v61
	v_med3_f32 v2, v2, s28, v61
	v_lshl_add_u64 v[34:35], v[46:47], 0, s[6:7]
	v_cvt_pk_fp8_f32 v5, v3, v2 op_sel:[0,0,1]
	global_store_dword v[30:31], v66, off nt
	global_store_dword v[34:35], v69, off nt
	global_store_dword v[30:31], v70, off offset:256 nt
	global_store_dword v[34:35], v71, off offset:256 nt
	global_store_dword v[30:31], v72, off offset:512 nt
	global_store_dword v[34:35], v73, off offset:512 nt
	global_store_dword v[30:31], v67, off offset:768 nt
	global_store_dword v[34:35], v36, off offset:768 nt
	global_store_dword v[30:31], v37, off offset:1024 nt
	global_store_dword v[34:35], v39, off offset:1024 nt
	global_store_dword v[30:31], v28, off offset:1280 nt
	global_store_dword v[34:35], v21, off offset:1280 nt
	global_store_dword v[30:31], v18, off offset:1536 nt
	global_store_dword v[34:35], v13, off offset:1536 nt
	global_store_dword v[30:31], v10, off offset:1792 nt
	global_store_dword v[34:35], v5, off offset:1792 nt
	s_and_saveexec_b64 s[26:27], s[4:5]
	s_cbranch_execz .LBB0_12
	s_waitcnt lgkmcnt(1)
	v_add_f32_e32 v2, v32, v33
	v_fmamk_f32 v2, v2, 0x3a000000, v62
	v_mul_f32_e32 v3, 0x4f800000, v2
	v_cmp_gt_f32_e32 vcc, s30, v2
	s_add_u32 s34, s82, s16
	s_addc_u32 s35, s83, s17
	v_cndmask_b32_e32 v2, v2, v3, vcc
	v_sqrt_f32_e32 v3, v2
	s_nop 0
	v_add_u32_e32 v4, -1, v3
	v_fma_f32 v6, -v4, v3, v2
	v_add_u32_e32 v5, 1, v3
	v_cmp_ge_f32_e64 s[6:7], 0, v6
	s_nop 1
	v_cndmask_b32_e64 v4, v3, v4, s[6:7]
	v_fma_f32 v3, -v5, v3, v2
	v_cmp_lt_f32_e64 s[6:7], 0, v3
	s_nop 1
	v_cndmask_b32_e64 v3, v4, v5, s[6:7]
	v_mul_f32_e32 v4, 0x37800000, v3
	v_cndmask_b32_e32 v3, v3, v4, vcc
	v_cmp_class_f32_e32 vcc, v2, v63
	s_waitcnt lgkmcnt(0)
	v_add_f32_e32 v5, v26, v27
	v_fmamk_f32 v5, v5, 0x3a000000, v62
	v_cndmask_b32_e32 v2, v3, v2, vcc
	v_div_scale_f32 v3, s[6:7], v2, v2, 1.0
	v_rcp_f32_e32 v4, v3
	v_mul_f32_e32 v8, 0x4f800000, v5
	v_cmp_gt_f32_e64 s[6:7], s30, v5
	v_fma_f32 v6, -v3, v4, 1.0
	s_nop 0
	v_cndmask_b32_e64 v5, v5, v8, s[6:7]
	v_fmac_f32_e32 v4, v6, v4
	v_div_scale_f32 v6, vcc, 1.0, v2, 1.0
	v_sqrt_f32_e32 v8, v5
	v_mul_f32_e32 v7, v6, v4
	v_fma_f32 v9, -v3, v7, v6
	v_fmac_f32_e32 v7, v9, v4
	v_fma_f32 v3, -v3, v7, v6
	v_add_u32_e32 v6, -1, v8
	v_fma_f32 v9, -v6, v8, v5
	v_cmp_ge_f32_e64 s[8:9], 0, v9
	v_add_u32_e32 v9, 1, v8
	v_div_fmas_f32 v3, v3, v4, v7
	v_cndmask_b32_e64 v6, v8, v6, s[8:9]
	v_fma_f32 v8, -v9, v8, v5
	v_cmp_lt_f32_e64 s[8:9], 0, v8
	v_div_fixup_f32 v2, v3, v2, 1.0
	global_store_dword v64, v2, s[34:35] nt
	v_cndmask_b32_e64 v6, v6, v9, s[8:9]
	v_mul_f32_e32 v8, 0x37800000, v6
	v_cndmask_b32_e64 v6, v6, v8, s[6:7]
	v_cmp_class_f32_e64 s[6:7], v5, v63
	s_nop 1
	v_cndmask_b32_e64 v5, v6, v5, s[6:7]
	v_div_scale_f32 v6, s[6:7], v5, v5, 1.0
	v_rcp_f32_e32 v8, v6
	s_nop 0
	v_fma_f32 v2, -v6, v8, 1.0
	v_fmac_f32_e32 v8, v2, v8
	v_div_scale_f32 v2, vcc, 1.0, v5, 1.0
	v_mul_f32_e32 v3, v2, v8
	v_fma_f32 v4, -v6, v3, v2
	v_fmac_f32_e32 v3, v4, v8
	v_fma_f32 v2, -v6, v3, v2
	v_div_fmas_f32 v2, v2, v8, v3
	v_div_fixup_f32 v2, v2, v5, 1.0
	global_store_dword v65, v2, s[34:35] nt
	s_branch .LBB0_12
